# grid barrier: per-XCD release counters added by every XCD leader (all-to-all), L1 invalidate issued by wave 1 at arrival so it overlaps the release chain
# speedup vs baseline: 1.0139x; 1.0139x over previous
.LBB0_42:
	v_readlane_b32 s2, v254, 7
	s_and_b32 s66, s22, 0xffffffc0
	v_readlane_b32 s3, v254, 8
	s_cmp_gt_i32 s3, 1
	s_cselect_b64 s[2:3], -1, 0
	s_and_b64 s[4:5], s[10:11], s[2:3]
	s_andn2_b64 vcc, exec, s[4:5]
	s_cbranch_vccnz .LBB0_96
	v_mbcnt_lo_u32_b32 v0, -1, 0
	v_mbcnt_hi_u32_b32 v0, -1, v0
	s_waitcnt vmcnt(0)
	s_nop 0
	v_or_b32_e32 v0, s66, v0
	v_cmp_eq_u32_e32 vcc, 0, v0
	s_barrier
	s_cmp_lg_u32 s66, 64
	s_cbranch_scc1 .Lmy_bar0_ni
	buffer_inv sc1
.Lmy_bar0_ni:
	s_and_saveexec_b64 s[4:5], vcc
	s_cbranch_execz .LBB0_95
	s_add_i32 s6, 0, 0x20160
	v_mov_b32_e32 v0, s6
	s_waitcnt vmcnt(0) expcnt(0) lgkmcnt(0)
	ds_read_b32 v2, v0
	s_add_i32 s6, 0, 0x20164
	v_mov_b32_e32 v0, s6
	ds_read_b32 v0, v0
	s_waitcnt lgkmcnt(1)
	v_cmp_ne_u32_e32 vcc, 0, v2
	s_cbranch_vccnz .LBB0_59
	v_readlane_b32 s6, v254, 0
	v_readlane_b32 s7, v254, 1
	s_load_dwordx2 s[8:9], s[6:7], 0x4
	v_readlane_b32 s6, v254, 4
	v_readlane_b32 s22, v254, 6
	v_readlane_b32 s7, v254, 5
	s_waitcnt lgkmcnt(0)
	s_mul_i32 s23, s8, s96
	s_add_u32 s8, s6, 0x1000
	s_mul_i32 s23, s23, s9
	s_addc_u32 s9, s7, 0
	s_add_u32 s10, s6, 0x1100
	s_addc_u32 s11, s7, 0
	s_add_u32 s12, s6, 0x1200
	s_addc_u32 s13, s7, 0
	s_add_u32 s14, s6, 0x1300
	s_addc_u32 s15, s7, 0
	s_mov_b32 s24, 1
	v_mov_b32_e32 v16, 0
	s_branch .LBB0_47

.LBB0_59:
	v_readlane_b32 s100, v254, 4
	v_readlane_b32 s101, v254, 5
	v_readlane_b32 vcc_lo, v254, 6
	v_mov_b32_e32 v3, 0x1000
	s_lshl_b32 vcc_lo, vcc_lo, 8
	v_mov_b32_e32 v4, 1
	v_add_u32_e32 v3, vcc_lo, v3
	v_mov_b32_e32 v1, 0x20160
	s_nop 4
	global_atomic_add v5, v3, v4, s[100:101] offset:1024 sc0
	ds_read_b32 v2, v1
	ds_read_b32 v1, v1 offset:4
	s_waitcnt lgkmcnt(0)
	v_cvt_f32_u32_e32 v0, v2
	v_rcp_f32_e32 v0, v0
	s_waitcnt vmcnt(0)
	v_readfirstlane_b32 vcc_hi, v5
	v_cvt_f32_u32_e32 v5, v5
	v_add_f32_e32 v5, 0.5, v5
	v_mul_f32_e32 v5, v5, v0
	v_cvt_u32_f32_e32 v5, v5
	v_add_u32_e32 v5, 1, v5
	v_mul_lo_u32 v0, v5, v2
	v_mul_lo_u32 v5, v5, v1
	s_add_u32 vcc_hi, vcc_hi, 1
	v_readfirstlane_b32 vcc_lo, v0
	v_add_u32_e32 v1, 0x1000, v3
	v_mov_b32_e32 v2, 0
	s_cmp_eq_u32 vcc_lo, vcc_hi
	s_cbranch_scc0 .Lmy_bar0_0_spin
	buffer_wbl2 sc1
	v_mov_b32_e32 v0, 0x2000
	v_mov_b32_e32 v3, 0x2800
	s_waitcnt vmcnt(0)
	global_atomic_add v0, v4, s[100:101] offset:1024
	global_atomic_add v0, v4, s[100:101] offset:1280
	global_atomic_add v0, v4, s[100:101] offset:1536
	global_atomic_add v0, v4, s[100:101] offset:1792
	global_atomic_add v0, v4, s[100:101] offset:2048
	global_atomic_add v0, v4, s[100:101] offset:2304
	global_atomic_add v0, v4, s[100:101] offset:2560
	global_atomic_add v0, v4, s[100:101] offset:2816
	global_atomic_add v3, v4, s[100:101] offset:1024
	global_atomic_add v3, v4, s[100:101] offset:1280
	global_atomic_add v3, v4, s[100:101] offset:1536
	global_atomic_add v3, v4, s[100:101] offset:1792
	global_atomic_add v3, v4, s[100:101] offset:2048
	global_atomic_add v3, v4, s[100:101] offset:2304
	global_atomic_add v3, v4, s[100:101] offset:2560
	global_atomic_add v3, v4, s[100:101] offset:2816
.Lmy_bar0_0_spin:
	global_load_dword v0, v1, s[100:101] offset:1024 sc1
	s_waitcnt vmcnt(0)
	v_cmp_ge_u32_e32 vcc, v0, v5
	s_cbranch_vccnz .Lmy_bar0_0_done
	s_sleep 1
	v_add_u32_e32 v2, 1, v2
	v_cmp_gt_u32_e32 vcc, 0x2000, v2
	s_cbranch_vccnz .Lmy_bar0_0_spin

.LBB0_95:
	s_or_b64 exec, exec, s[4:5]
	s_waitcnt vmcnt(0) lgkmcnt(0)
	s_barrier

.LBB0_177:
	v_readlane_b32 s2, v254, 7
	v_readlane_b32 s3, v254, 8
	s_cmp_gt_u32 s3, 2
	s_cselect_b64 s[2:3], -1, 0
	s_and_b64 s[2:3], s[14:15], s[2:3]
	s_andn2_b64 vcc, exec, s[2:3]
	s_cbranch_vccnz .LBB0_231
	s_waitcnt vmcnt(0)
	v_mbcnt_lo_u32_b32 v0, -1, 0
	v_mbcnt_hi_u32_b32 v0, -1, v0
	s_waitcnt vmcnt(0)
	s_nop 0
	v_or_b32_e32 v0, s66, v0
	v_cmp_eq_u32_e32 vcc, 0, v0
	s_barrier
	s_cmp_lg_u32 s66, 64
	s_cbranch_scc1 .Lmy_bar1_ni
	buffer_inv sc1
.Lmy_bar1_ni:
	s_and_saveexec_b64 s[2:3], vcc
	s_cbranch_execz .LBB0_230
	s_add_i32 s4, 0, 0x20160
	v_mov_b32_e32 v0, s4
	s_waitcnt vmcnt(0) expcnt(0) lgkmcnt(0)
	ds_read_b32 v2, v0
	s_add_i32 s4, 0, 0x20164
	v_mov_b32_e32 v0, s4
	ds_read_b32 v0, v0
	s_waitcnt lgkmcnt(1)
	v_cmp_ne_u32_e32 vcc, 0, v2
	s_cbranch_vccnz .LBB0_194
	v_readlane_b32 s4, v254, 0
	v_readlane_b32 s5, v254, 1
	s_load_dwordx2 s[6:7], s[4:5], 0x4
	v_readlane_b32 s4, v254, 4
	v_readlane_b32 s22, v254, 6
	v_readlane_b32 s5, v254, 5
	s_waitcnt lgkmcnt(0)
	s_mul_i32 s23, s6, s96
	s_add_u32 s6, s4, 0x1000
	s_mul_i32 s23, s23, s7
	s_addc_u32 s7, s5, 0
	s_add_u32 s8, s4, 0x1100
	s_addc_u32 s9, s5, 0
	s_add_u32 s10, s4, 0x1200
	s_addc_u32 s11, s5, 0
	s_add_u32 s14, s4, 0x1300
	s_addc_u32 s15, s5, 0
	s_mov_b32 s24, 1
	v_mov_b32_e32 v16, 0
	s_branch .LBB0_182

.LBB0_230:
	s_or_b64 exec, exec, s[2:3]
	s_waitcnt vmcnt(0) lgkmcnt(0)
	s_barrier

.LBB0_244:
	v_readlane_b32 s4, v254, 7
	s_or_b32 s24, s67, 3
	v_readlane_b32 s5, v254, 8
	s_cmp_ge_i32 s24, s5
	s_cbranch_scc1 .LBB0_298
	v_mbcnt_lo_u32_b32 v0, -1, 0
	v_mbcnt_hi_u32_b32 v0, -1, v0
	s_waitcnt vmcnt(0)
	s_nop 0
	v_or_b32_e32 v0, s66, v0
	v_cmp_eq_u32_e32 vcc, 0, v0
	s_barrier
	s_cmp_lg_u32 s66, 64
	s_cbranch_scc1 .Lmy_bar2_ni
	buffer_inv sc1
.Lmy_bar2_ni:
	s_and_saveexec_b64 s[4:5], vcc
	s_cbranch_execz .LBB0_297
	v_readlane_b32 s6, v255, 14
	s_waitcnt vmcnt(0) expcnt(0) lgkmcnt(0)
	s_nop 0
	v_mov_b32_e32 v0, s6
	ds_read_b32 v2, v0
	v_readlane_b32 s6, v255, 15
	s_waitcnt lgkmcnt(0)
	v_cmp_ne_u32_e32 vcc, 0, v2
	v_mov_b32_e32 v0, s6
	ds_read_b32 v0, v0
	s_cbranch_vccnz .LBB0_261
	v_readlane_b32 s6, v254, 0
	v_readlane_b32 s7, v254, 1
	s_load_dwordx2 s[8:9], s[6:7], 0x4
	v_readlane_b32 s6, v254, 4
	v_readlane_b32 s25, v254, 6
	v_readlane_b32 s7, v254, 5
	s_waitcnt lgkmcnt(0)
	s_mul_i32 s26, s8, s96
	s_add_u32 s8, s6, 0x1000
	s_mul_i32 s26, s26, s9
	s_addc_u32 s9, s7, 0
	s_add_u32 s10, s6, 0x1100
	s_addc_u32 s11, s7, 0
	s_add_u32 s14, s6, 0x1200
	s_addc_u32 s15, s7, 0
	s_add_u32 s16, s6, 0x1300
	s_addc_u32 s17, s7, 0
	s_mov_b32 s27, 1
	s_branch .LBB0_249

.LBB0_261:
	v_readlane_b32 s100, v254, 4
	v_readlane_b32 s101, v254, 5
	v_readlane_b32 vcc_lo, v254, 6
	v_mov_b32_e32 v3, 0x1000
	s_lshl_b32 vcc_lo, vcc_lo, 8
	v_mov_b32_e32 v4, 1
	v_add_u32_e32 v3, vcc_lo, v3
	v_mov_b32_e32 v1, 0x20160
	s_nop 4
	global_atomic_add v5, v3, v4, s[100:101] offset:1024 sc0
	ds_read_b32 v2, v1
	ds_read_b32 v1, v1 offset:4
	s_waitcnt lgkmcnt(0)
	v_cvt_f32_u32_e32 v6, v2
	v_rcp_f32_e32 v6, v6
	s_waitcnt vmcnt(0)
	v_readfirstlane_b32 vcc_hi, v5
	v_cvt_f32_u32_e32 v5, v5
	v_add_f32_e32 v5, 0.5, v5
	v_mul_f32_e32 v5, v5, v6
	v_cvt_u32_f32_e32 v5, v5
	v_add_u32_e32 v5, 1, v5
	v_mul_lo_u32 v6, v5, v2
	v_mul_lo_u32 v5, v5, v1
	s_add_u32 vcc_hi, vcc_hi, 1
	v_readfirstlane_b32 vcc_lo, v6
	v_add_u32_e32 v1, 0x1000, v3
	v_mov_b32_e32 v2, 0
	s_cmp_eq_u32 vcc_lo, vcc_hi
	s_cbranch_scc0 .Lmy_bar2_0_spin
	buffer_wbl2 sc1
	v_mov_b32_e32 v6, 0x2000
	v_mov_b32_e32 v3, 0x2800
	s_waitcnt vmcnt(0)
	global_atomic_add v6, v4, s[100:101] offset:1024
	global_atomic_add v6, v4, s[100:101] offset:1280
	global_atomic_add v6, v4, s[100:101] offset:1536
	global_atomic_add v6, v4, s[100:101] offset:1792
	global_atomic_add v6, v4, s[100:101] offset:2048
	global_atomic_add v6, v4, s[100:101] offset:2304
	global_atomic_add v6, v4, s[100:101] offset:2560
	global_atomic_add v6, v4, s[100:101] offset:2816
	global_atomic_add v3, v4, s[100:101] offset:1024
	global_atomic_add v3, v4, s[100:101] offset:1280
	global_atomic_add v3, v4, s[100:101] offset:1536
	global_atomic_add v3, v4, s[100:101] offset:1792
	global_atomic_add v3, v4, s[100:101] offset:2048
	global_atomic_add v3, v4, s[100:101] offset:2304
	global_atomic_add v3, v4, s[100:101] offset:2560
	global_atomic_add v3, v4, s[100:101] offset:2816
.Lmy_bar2_0_spin:
	global_load_dword v6, v1, s[100:101] offset:1024 sc1
	s_waitcnt vmcnt(0)
	v_cmp_ge_u32_e32 vcc, v6, v5
	s_cbranch_vccnz .Lmy_bar2_0_done
	s_sleep 1
	v_add_u32_e32 v2, 1, v2
	v_cmp_gt_u32_e32 vcc, 0x2000, v2
	s_cbranch_vccnz .Lmy_bar2_0_spin

.LBB0_668:
	v_readlane_b32 s2, v254, 7
	s_add_i32 s22, s67, 4
	v_readlane_b32 s3, v254, 8
	s_cmp_lt_i32 s22, s3
	s_cselect_b64 s[2:3], -1, 0
	s_and_b64 s[4:5], s[4:5], s[2:3]
	s_andn2_b64 vcc, exec, s[4:5]
	s_cbranch_vccnz .LBB0_722
	s_waitcnt vmcnt(0)
	v_mbcnt_lo_u32_b32 v0, -1, 0
	v_mbcnt_hi_u32_b32 v0, -1, v0
	s_waitcnt vmcnt(0)
	s_nop 0
	v_or_b32_e32 v0, s66, v0
	v_cmp_eq_u32_e32 vcc, 0, v0
	s_barrier
	s_cmp_lg_u32 s66, 64
	s_cbranch_scc1 .Lmy_bar3_ni
	buffer_inv sc1
.Lmy_bar3_ni:
	s_and_saveexec_b64 s[4:5], vcc
	s_cbranch_execz .LBB0_721
	v_readlane_b32 s6, v255, 14
	s_waitcnt vmcnt(0) expcnt(0) lgkmcnt(0)
	s_nop 0
	v_mov_b32_e32 v0, s6
	ds_read_b32 v2, v0
	v_readlane_b32 s6, v255, 15
	s_waitcnt lgkmcnt(0)
	v_cmp_ne_u32_e32 vcc, 0, v2
	v_mov_b32_e32 v0, s6
	ds_read_b32 v0, v0
	s_cbranch_vccnz .LBB0_685
	v_readlane_b32 s6, v254, 0
	v_readlane_b32 s7, v254, 1
	s_load_dwordx2 s[8:9], s[6:7], 0x4
	v_readlane_b32 s6, v254, 4
	v_readlane_b32 s23, v254, 6
	v_readlane_b32 s7, v254, 5
	s_waitcnt lgkmcnt(0)
	s_mul_i32 s24, s8, s96
	s_add_u32 s8, s6, 0x1000
	s_mul_i32 s24, s24, s9
	s_addc_u32 s9, s7, 0
	s_add_u32 s10, s6, 0x1100
	s_addc_u32 s11, s7, 0
	s_add_u32 s12, s6, 0x1200
	s_addc_u32 s13, s7, 0
	s_add_u32 s14, s6, 0x1300
	s_addc_u32 s15, s7, 0
	s_mov_b32 s25, 1
	s_branch .LBB0_673

.LBB0_755:
	v_readlane_b32 s2, v254, 7
	s_add_i32 s20, s67, 5
	v_readlane_b32 s3, v254, 8
	s_cmp_ge_i32 s20, s3
	s_cbranch_scc1 .LBB0_809
	v_mbcnt_lo_u32_b32 v0, -1, 0
	v_mbcnt_hi_u32_b32 v0, -1, v0
	s_waitcnt vmcnt(0)
	s_nop 0
	v_or_b32_e32 v0, s66, v0
	v_cmp_eq_u32_e32 vcc, 0, v0
	s_barrier
	s_cmp_lg_u32 s66, 64
	s_cbranch_scc1 .Lmy_bar4_ni
	buffer_inv sc1
.Lmy_bar4_ni:
	s_and_saveexec_b64 s[2:3], vcc
	s_cbranch_execz .LBB0_808
	v_readlane_b32 s4, v255, 14
	s_waitcnt vmcnt(0) expcnt(0) lgkmcnt(0)
	s_nop 0
	v_mov_b32_e32 v0, s4
	ds_read_b32 v2, v0
	v_readlane_b32 s4, v255, 15
	s_waitcnt lgkmcnt(0)
	v_cmp_ne_u32_e32 vcc, 0, v2
	v_mov_b32_e32 v0, s4
	ds_read_b32 v0, v0
	s_cbranch_vccnz .LBB0_772
	v_readlane_b32 s4, v254, 0
	v_readlane_b32 s5, v254, 1
	s_load_dwordx2 s[6:7], s[4:5], 0x4
	v_readlane_b32 s4, v254, 4
	v_readlane_b32 s21, v254, 6
	v_readlane_b32 s5, v254, 5
	s_waitcnt lgkmcnt(0)
	s_mul_i32 s22, s6, s96
	s_add_u32 s6, s4, 0x1000
	s_mul_i32 s22, s22, s7
	s_addc_u32 s7, s5, 0
	s_add_u32 s8, s4, 0x1100
	s_addc_u32 s9, s5, 0
	s_add_u32 s10, s4, 0x1200
	s_addc_u32 s11, s5, 0
	s_add_u32 s12, s4, 0x1300
	s_addc_u32 s13, s5, 0
	s_mov_b32 s23, 1
	s_branch .LBB0_760

.LBB0_934:
	s_add_i32 s22, s67, 6
	s_cmp_lt_i32 s22, s95
	s_cselect_b64 s[2:3], -1, 0
	s_and_b64 s[4:5], s[46:47], s[2:3]
	s_andn2_b64 vcc, exec, s[4:5]
	s_cbranch_vccnz .LBB0_988
	v_mbcnt_lo_u32_b32 v0, -1, 0
	v_mbcnt_hi_u32_b32 v0, -1, v0
	s_waitcnt vmcnt(0)
	s_nop 0
	v_or_b32_e32 v0, s66, v0
	v_cmp_eq_u32_e32 vcc, 0, v0
	s_barrier
	s_cmp_lg_u32 s66, 64
	s_cbranch_scc1 .Lmy_bar5_ni
	buffer_inv sc1

.LBB0_994:
	s_or_b64 exec, exec, s[2:3]
	v_readlane_b32 s2, v254, 7
	s_add_i32 s20, s67, 7
	v_readlane_b32 s3, v254, 8
	s_cmp_ge_i32 s20, s3
	s_cbranch_scc1 .LBB0_1048
	v_mbcnt_lo_u32_b32 v0, -1, 0
	v_mbcnt_hi_u32_b32 v0, -1, v0
	s_waitcnt vmcnt(0)
	s_nop 0
	v_or_b32_e32 v0, s66, v0
	v_cmp_eq_u32_e32 vcc, 0, v0
	s_barrier
	s_cmp_lg_u32 s66, 64
	s_cbranch_scc1 .Lmy_bar6_ni
	buffer_inv sc1

.LBB0_1062:
	v_readlane_b32 s2, v254, 7
	s_add_i32 s20, s67, 8
	v_readlane_b32 s3, v254, 8
	s_cmp_ge_i32 s20, s3
	s_barrier
	s_cbranch_scc1 .LBB0_1116
	v_mbcnt_lo_u32_b32 v0, -1, 0
	v_mbcnt_hi_u32_b32 v0, -1, v0
	s_waitcnt vmcnt(0)
	s_nop 0
	v_or_b32_e32 v0, s66, v0
	v_cmp_eq_u32_e32 vcc, 0, v0
	s_barrier
	s_cmp_lg_u32 s66, 64
	s_cbranch_scc1 .Lmy_bar7_ni
	buffer_inv sc1

.LBB0_1301:
	v_readlane_b32 s2, v254, 7
	s_add_i32 s22, s67, 9
	v_readlane_b32 s3, v254, 8
	s_cmp_lt_i32 s22, s3
	s_cselect_b64 s[2:3], -1, 0
	s_and_b64 s[4:5], s[4:5], s[2:3]
	s_andn2_b64 vcc, exec, s[4:5]
	s_cbranch_vccnz .LBB0_1355
	s_waitcnt vmcnt(0)
	v_mbcnt_lo_u32_b32 v0, -1, 0
	v_mbcnt_hi_u32_b32 v0, -1, v0
	s_waitcnt vmcnt(0)
	s_nop 0
	v_or_b32_e32 v0, s66, v0
	v_cmp_eq_u32_e32 vcc, 0, v0
	s_barrier
	s_cmp_lg_u32 s66, 64
	s_cbranch_scc1 .Lmy_bar8_ni
	buffer_inv sc1

.LBB0_1474:
	v_readlane_b32 s2, v254, 7
	s_add_i32 s22, s67, 10
	v_readlane_b32 s3, v254, 8
	s_cmp_lt_i32 s22, s3
	s_cselect_b64 s[2:3], -1, 0
	s_and_b64 s[4:5], s[4:5], s[2:3]
	s_andn2_b64 vcc, exec, s[4:5]
	s_cbranch_vccnz .LBB0_1528
	s_waitcnt vmcnt(0)
	v_mbcnt_lo_u32_b32 v0, -1, 0
	v_mbcnt_hi_u32_b32 v0, -1, v0
	s_waitcnt vmcnt(0)
	s_nop 0
	v_or_b32_e32 v0, s66, v0
	v_cmp_eq_u32_e32 vcc, 0, v0
	s_barrier
	s_cmp_lg_u32 s66, 64
	s_cbranch_scc1 .Lmy_bar9_ni
	buffer_inv sc1

.LBB0_1549:
	v_readlane_b32 s4, v254, 7
	s_add_i32 s22, s67, 11
	v_readlane_b32 s5, v254, 8
	s_cmp_ge_i32 s22, s5
	s_cbranch_scc1 .LBB0_1603
	v_mbcnt_lo_u32_b32 v0, -1, 0
	v_mbcnt_hi_u32_b32 v0, -1, v0
	s_waitcnt vmcnt(0)
	s_nop 0
	v_or_b32_e32 v0, s66, v0
	v_cmp_eq_u32_e32 vcc, 0, v0
	s_barrier
	s_cmp_lg_u32 s66, 64
	s_cbranch_scc1 .Lmy_bar10_ni
	buffer_inv sc1

.LBB0_1709:
	s_and_b64 vcc, exec, s[4:5]
	s_cbranch_vccz .LBB0_1767
	v_readlane_b32 s4, v255, 35
	v_readlane_b32 s5, v255, 36
	s_andn2_b64 vcc, exec, s[4:5]
	s_cbranch_vccnz .LBB0_1767
	v_readlane_b32 s6, v254, 7
	s_add_i32 s4, s67, 12
	v_readlane_b32 s7, v254, 8
	s_cmp_lt_i32 s4, s7
	s_cselect_b64 s[4:5], -1, 0
	s_and_b64 s[4:5], s[8:9], s[4:5]
	s_andn2_b64 vcc, exec, s[4:5]
	s_cbranch_vccnz .LBB0_1766
	v_mbcnt_lo_u32_b32 v0, -1, 0
	v_mbcnt_hi_u32_b32 v0, -1, v0
	s_waitcnt vmcnt(0)
	s_nop 0
	v_or_b32_e32 v0, s66, v0
	v_cmp_eq_u32_e32 vcc, 0, v0
	s_barrier
	s_cmp_lg_u32 s66, 64
	s_cbranch_scc1 .Lmy_bar11_ni
	buffer_inv sc1
.Lmy_bar11_ni:
	s_and_saveexec_b64 s[4:5], vcc
	s_cbranch_execz .LBB0_1765
	v_readlane_b32 s6, v255, 14
	s_waitcnt vmcnt(0) expcnt(0) lgkmcnt(0)
	s_nop 0
	v_mov_b32_e32 v0, s6
	ds_read_b32 v2, v0
	v_readlane_b32 s6, v255, 15
	s_waitcnt lgkmcnt(0)
	v_cmp_ne_u32_e32 vcc, 0, v2
	v_mov_b32_e32 v0, s6
	ds_read_b32 v0, v0
	s_cbranch_vccnz .LBB0_1729
	v_readlane_b32 s6, v254, 0
	v_readlane_b32 s7, v254, 1
	s_load_dwordx2 s[8:9], s[6:7], 0x4
	v_readlane_b32 s6, v254, 4
	v_readlane_b32 s22, v254, 6
	v_readlane_b32 s7, v254, 5
	s_waitcnt lgkmcnt(0)
	s_mul_i32 s23, s8, s96
	s_add_u32 s8, s6, 0x1000
	s_mul_i32 s23, s23, s9
	s_addc_u32 s9, s7, 0
	s_add_u32 s10, s6, 0x1100
	s_addc_u32 s11, s7, 0
	s_add_u32 s12, s6, 0x1200
	s_addc_u32 s13, s7, 0
	s_add_u32 s14, s6, 0x1300
	s_addc_u32 s15, s7, 0
	s_mov_b32 s24, 1
	s_branch .LBB0_1716

.LBB0_1887:
	v_readlane_b32 s2, v254, 7
	s_add_i32 s26, s67, 13
	v_readlane_b32 s3, v254, 8
	s_cmp_lt_i32 s26, s3
	s_cselect_b64 s[2:3], -1, 0
	s_and_b64 s[6:7], s[4:5], s[2:3]
	s_andn2_b64 vcc, exec, s[6:7]
	s_cbranch_vccnz .LBB0_1941
	s_waitcnt vmcnt(0)
	v_mbcnt_lo_u32_b32 v0, -1, 0
	v_mbcnt_hi_u32_b32 v0, -1, v0
	s_waitcnt vmcnt(0)
	s_nop 0
	v_or_b32_e32 v0, s66, v0
	v_cmp_eq_u32_e32 vcc, 0, v0
	s_barrier
	s_cmp_lg_u32 s66, 64
	s_cbranch_scc1 .Lmy_bar12_ni
	buffer_inv sc1
.Lmy_bar12_ni:
	s_and_saveexec_b64 s[6:7], vcc
	s_cbranch_execz .LBB0_1940
	v_readlane_b32 s8, v255, 14
	s_waitcnt vmcnt(0) expcnt(0) lgkmcnt(0)
	s_nop 0
	v_mov_b32_e32 v0, s8
	ds_read_b32 v2, v0
	v_readlane_b32 s8, v255, 15
	s_waitcnt lgkmcnt(0)
	v_cmp_ne_u32_e32 vcc, 0, v2
	v_mov_b32_e32 v0, s8
	ds_read_b32 v0, v0
	s_cbranch_vccnz .LBB0_1904
	v_readlane_b32 s8, v254, 0
	v_readlane_b32 s9, v254, 1
	s_load_dwordx2 s[10:11], s[8:9], 0x4
	v_readlane_b32 s8, v254, 4
	v_readlane_b32 s27, v254, 6
	v_readlane_b32 s9, v254, 5
	s_waitcnt lgkmcnt(0)
	s_mul_i32 s28, s10, s96
	s_add_u32 s10, s8, 0x1000
	s_mul_i32 s28, s28, s11
	s_addc_u32 s11, s9, 0
	s_add_u32 s14, s8, 0x1100
	s_addc_u32 s15, s9, 0
	s_add_u32 s16, s8, 0x1200
	s_addc_u32 s17, s9, 0
	s_add_u32 s18, s8, 0x1300
	s_addc_u32 s19, s9, 0
	s_mov_b32 s29, 1
	s_branch .LBB0_1892

.LBB0_1940:
	s_or_b64 exec, exec, s[6:7]
	s_waitcnt vmcnt(0) lgkmcnt(0)
	s_barrier

.LBB0_2059:
	v_readlane_b32 s8, v254, 7
	s_add_i32 s2, s67, 14
	v_readlane_b32 s9, v254, 8
	s_cmp_lt_i32 s2, s9
	s_cselect_b64 s[2:3], -1, 0
	s_and_b64 s[2:3], s[6:7], s[2:3]
	s_andn2_b64 vcc, exec, s[2:3]
	s_mov_b32 s88, s71
	s_mov_b32 s55, 0x80000
	s_mov_b32 s91, 0x90000
	s_mov_b32 s92, 0xa0000
	s_mov_b32 s93, 0xb0000
	s_cbranch_vccnz .LBB0_2113
	s_waitcnt vmcnt(0)
	v_mbcnt_lo_u32_b32 v0, -1, 0
	v_mbcnt_hi_u32_b32 v0, -1, v0
	s_waitcnt vmcnt(0)
	s_nop 0
	v_or_b32_e32 v0, s66, v0
	v_cmp_eq_u32_e32 vcc, 0, v0
	s_barrier
	s_cmp_lg_u32 s66, 64
	s_cbranch_scc1 .Lmy_bar13_ni
	buffer_inv sc1
.Lmy_bar13_ni:
	s_and_saveexec_b64 s[2:3], vcc
	s_cbranch_execz .LBB0_2112
	v_readlane_b32 s6, v255, 14
	s_waitcnt vmcnt(0) expcnt(0) lgkmcnt(0)
	s_nop 0
	v_mov_b32_e32 v0, s6
	ds_read_b32 v2, v0
	v_readlane_b32 s6, v255, 15
	s_waitcnt lgkmcnt(0)
	v_cmp_ne_u32_e32 vcc, 0, v2
	v_mov_b32_e32 v0, s6
	ds_read_b32 v0, v0
	s_cbranch_vccnz .LBB0_2076
	v_readlane_b32 s6, v254, 0
	v_readlane_b32 s7, v254, 1
	s_load_dwordx2 s[8:9], s[6:7], 0x4
	v_readlane_b32 s6, v254, 4
	v_readlane_b32 s24, v254, 6
	v_readlane_b32 s7, v254, 5
	s_waitcnt lgkmcnt(0)
	s_mul_i32 s25, s8, s96
	s_add_u32 s8, s6, 0x1000
	s_mul_i32 s25, s25, s9
	s_addc_u32 s9, s7, 0
	s_add_u32 s10, s6, 0x1100
	s_addc_u32 s11, s7, 0
	s_add_u32 s14, s6, 0x1200
	s_addc_u32 s15, s7, 0
	s_add_u32 s16, s6, 0x1300
	s_addc_u32 s17, s7, 0
	s_mov_b32 s26, 1
	s_branch .LBB0_2064

.LBB0_2136:
	v_readlane_b32 s2, v254, 7
	s_add_i32 s20, s67, 13
	v_readlane_b32 s3, v254, 8
	s_cmp_ge_i32 s20, s3
	s_cbranch_scc1 .LBB0_2190
	v_mbcnt_lo_u32_b32 v0, -1, 0
	v_mbcnt_hi_u32_b32 v0, -1, v0
	s_waitcnt vmcnt(0)
	s_waitcnt vmcnt(0)
	v_or_b32_e32 v0, s66, v0
	v_cmp_eq_u32_e32 vcc, 0, v0
	s_barrier
	s_cmp_lg_u32 s66, 64
	s_cbranch_scc1 .Lmy_bar14_ni
	buffer_inv sc1

.LBB0_2240:
	v_mbcnt_lo_u32_b32 v0, -1, 0
	v_mbcnt_hi_u32_b32 v0, -1, v0
	s_waitcnt vmcnt(0)
	s_waitcnt vmcnt(0) lgkmcnt(0)
	v_or_b32_e32 v0, s66, v0
	v_cmp_eq_u32_e32 vcc, 0, v0
	s_barrier
	s_cmp_lg_u32 s66, 64
	s_cbranch_scc1 .Lmy_bar15_ni
	buffer_inv sc1
.Lmy_bar15_ni:
	s_and_saveexec_b64 s[2:3], vcc
	s_cbranch_execnz .LBB0_2241
	s_getpc_b64 s[98:99]

.Lmy_bar15_0_done:
	s_waitcnt vmcnt(0)
	s_mov_b64 s[6:7], 0
	s_getpc_b64 s[98:99]
